# speedup vs baseline: 1.0239x; 1.0057x over previous
_Z9ln_kernelILi2EEvPKiPKfS3_PfS3_S3_PDF16_:
	s_load_dwordx4 s[12:15], s[0:1], 0x20
	v_and_b32_e32 v62, 63, v0
	v_lshlrev_b32_e32 v62, 4, v62
	s_load_dwordx8 s[4:11], s[0:1], 0x8
	v_and_b32_e32 v12, 63, v0
	v_lshrrev_b32_e32 v0, 6, v0
	v_lshl_or_b32 v6, s2, 2, v0
	v_ashrrev_i32_e32 v7, 31, v6
	v_lshlrev_b64 v[2:3], 11, v[6:7]
	v_mov_b32_e32 v1, 0
	s_waitcnt lgkmcnt(0)
	v_lshl_add_u64 v[8:9], s[4:5], 0, v[2:3]
	v_lshlrev_b32_e32 v4, 3, v12
	v_mov_b32_e32 v5, v1
	v_lshl_add_u64 v[8:9], v[8:9], 0, v[4:5]
	s_mov_b64 s[2:3], 0x400000
	v_lshl_add_u64 v[10:11], v[8:9], 0, s[2:3]
	s_mov_b32 s2, 0x400000
	global_load_dwordx2 v[16:17], v[8:9], off
	global_load_dwordx2 v[18:19], v[8:9], off offset:512
	global_load_dwordx2 v[20:21], v[8:9], off offset:1024
	global_load_dwordx2 v[22:23], v[8:9], off offset:1536
	v_add_co_u32_e32 v8, vcc, s2, v8
	global_load_dwordx2 v[24:25], v[10:11], off offset:512
	global_load_dwordx2 v[26:27], v[10:11], off offset:1024
	global_load_dwordx2 v[28:29], v[10:11], off offset:1536
	v_addc_co_u32_e32 v9, vcc, 0, v9, vcc
	global_load_dwordx2 v[30:31], v[8:9], off
	v_lshlrev_b64 v[6:7], 12, v[6:7]
	v_lshlrev_b32_e32 v0, 4, v12
	v_lshl_add_u64 v[6:7], s[8:9], 0, v[6:7]
	v_lshl_add_u64 v[6:7], v[6:7], 0, v[0:1]
	global_load_dwordx4 v[8:11], v[6:7], off offset:1024
	global_load_dwordx4 v[12:15], v0, s[6:7] offset:1024
	s_waitcnt vmcnt(9)
	v_cvt_f32_f16_e32 v32, v16
	s_waitcnt vmcnt(8)
	v_cvt_f32_f16_e32 v36, v18
	v_cvt_f32_f16_sdwa v37, v18 dst_sel:DWORD dst_unused:UNUSED_PAD src0_sel:WORD_1
	v_cvt_f32_f16_e32 v38, v19
	v_cvt_f32_f16_sdwa v39, v19 dst_sel:DWORD dst_unused:UNUSED_PAD src0_sel:WORD_1
	s_waitcnt vmcnt(7)
	v_cvt_f32_f16_e32 v40, v20
	v_cvt_f32_f16_sdwa v41, v20 dst_sel:DWORD dst_unused:UNUSED_PAD src0_sel:WORD_1
	v_cvt_f32_f16_e32 v42, v21
	v_cvt_f32_f16_sdwa v43, v21 dst_sel:DWORD dst_unused:UNUSED_PAD src0_sel:WORD_1
	s_waitcnt vmcnt(6)
	v_cvt_f32_f16_e32 v44, v22
	v_cvt_f32_f16_sdwa v45, v22 dst_sel:DWORD dst_unused:UNUSED_PAD src0_sel:WORD_1
	v_cvt_f32_f16_e32 v46, v23
	v_cvt_f32_f16_sdwa v47, v23 dst_sel:DWORD dst_unused:UNUSED_PAD src0_sel:WORD_1
	s_waitcnt vmcnt(5)
	v_cvt_f32_f16_e32 v20, v24
	v_cvt_f32_f16_sdwa v21, v24 dst_sel:DWORD dst_unused:UNUSED_PAD src0_sel:WORD_1
	v_cvt_f32_f16_e32 v22, v25
	v_cvt_f32_f16_sdwa v23, v25 dst_sel:DWORD dst_unused:UNUSED_PAD src0_sel:WORD_1
	s_waitcnt vmcnt(4)
	v_cvt_f32_f16_e32 v24, v26
	v_cvt_f32_f16_sdwa v25, v26 dst_sel:DWORD dst_unused:UNUSED_PAD src0_sel:WORD_1
	v_cvt_f32_f16_e32 v26, v27
	v_cvt_f32_f16_sdwa v27, v27 dst_sel:DWORD dst_unused:UNUSED_PAD src0_sel:WORD_1
	s_waitcnt vmcnt(3)
	v_cvt_f32_f16_e32 v48, v28
	v_cvt_f32_f16_sdwa v49, v28 dst_sel:DWORD dst_unused:UNUSED_PAD src0_sel:WORD_1
	v_cvt_f32_f16_e32 v28, v29
	v_cvt_f32_f16_sdwa v29, v29 dst_sel:DWORD dst_unused:UNUSED_PAD src0_sel:WORD_1
	v_cvt_f32_f16_sdwa v33, v16 dst_sel:DWORD dst_unused:UNUSED_PAD src0_sel:WORD_1
	v_cvt_f32_f16_e32 v34, v17
	v_cvt_f32_f16_sdwa v35, v17 dst_sel:DWORD dst_unused:UNUSED_PAD src0_sel:WORD_1
	s_waitcnt vmcnt(2)
	v_cvt_f32_f16_e32 v50, v30
	v_cvt_f32_f16_sdwa v51, v30 dst_sel:DWORD dst_unused:UNUSED_PAD src0_sel:WORD_1
	v_cvt_f32_f16_e32 v52, v31
	v_cvt_f32_f16_sdwa v53, v31 dst_sel:DWORD dst_unused:UNUSED_PAD src0_sel:WORD_1
	global_load_dwordx4 v[16:19], v[6:7], off
	v_pk_add_f32 v[36:37], v[36:37], v[20:21]
	v_pk_add_f32 v[38:39], v[38:39], v[22:23]
	global_load_dwordx4 v[20:23], v[6:7], off offset:2048
	v_pk_add_f32 v[40:41], v[40:41], v[24:25]
	v_pk_add_f32 v[42:43], v[42:43], v[26:27]
	global_load_dwordx4 v[24:27], v[6:7], off offset:3072
	v_pk_add_f32 v[46:47], v[46:47], v[28:29]
	global_load_dwordx4 v[28:31], v0, s[6:7] offset:2048
	s_waitcnt vmcnt(5)
	v_pk_add_f32 v[36:37], v[8:9], v[36:37]
	v_pk_add_f32 v[38:39], v[10:11], v[38:39]
	global_load_dwordx4 v[8:11], v0, s[6:7]
	v_pk_add_f32 v[44:45], v[44:45], v[48:49]
	v_pk_add_f32 v[48:49], v[32:33], v[50:51]
	v_pk_add_f32 v[50:51], v[34:35], v[52:53]
	global_load_dwordx4 v[32:35], v0, s[6:7] offset:3072
	global_load_dwordx4 v[64:67], v62, s[12:13]
	global_load_dwordx4 v[68:71], v62, s[12:13] offset:1024
	global_load_dwordx4 v[72:75], v62, s[12:13] offset:2048
	global_load_dwordx4 v[76:79], v62, s[12:13] offset:3072
	global_load_dwordx4 v[80:83], v62, s[14:15]
	global_load_dwordx4 v[84:87], v62, s[14:15] offset:1024
	global_load_dwordx4 v[88:91], v62, s[14:15] offset:2048
	global_load_dwordx4 v[92:95], v62, s[14:15] offset:3072
	s_waitcnt vmcnt(14)
	v_pk_add_f32 v[12:13], v[12:13], v[36:37]
	v_pk_add_f32 v[14:15], v[14:15], v[38:39]
	s_load_dwordx4 s[4:7], s[0:1], 0x28
	s_mov_b32 s0, 0xf800000
	s_waitcnt lgkmcnt(0)
	v_lshl_add_u64 v[2:3], s[6:7], 0, v[2:3]
	s_waitcnt vmcnt(12)
	v_pk_add_f32 v[20:21], v[20:21], v[40:41]
	v_pk_add_f32 v[22:23], v[22:23], v[42:43]
	v_pk_add_f32 v[40:41], v[16:17], v[48:49]
	v_pk_add_f32 v[42:43], v[18:19], v[50:51]
	s_waitcnt vmcnt(11)
	v_pk_add_f32 v[24:25], v[24:25], v[44:45]
	v_pk_add_f32 v[26:27], v[26:27], v[46:47]
	s_waitcnt vmcnt(10)
	v_pk_add_f32 v[16:17], v[28:29], v[20:21]
	v_pk_add_f32 v[18:19], v[30:31], v[22:23]
	s_waitcnt vmcnt(9)
	v_pk_add_f32 v[8:9], v[8:9], v[40:41]
	v_pk_add_f32 v[10:11], v[10:11], v[42:43]
	v_mov_b32_e32 v28, v13
	v_mov_b32_e32 v29, v15
	s_waitcnt vmcnt(8)
	v_pk_add_f32 v[20:21], v[32:33], v[24:25]
	v_pk_add_f32 v[22:23], v[34:35], v[26:27]
	v_mov_b32_e32 v24, v8
	v_mov_b32_e32 v25, v10
	v_mov_b32_e32 v26, v9
	v_mov_b32_e32 v27, v11
	v_pk_add_f32 v[24:25], v[24:25], v[26:27]
	v_mov_b32_e32 v26, v12
	v_mov_b32_e32 v27, v14
	v_pk_add_f32 v[26:27], v[26:27], v[28:29]
	v_add_f32_e32 v1, v24, v25
	v_pk_add_f32 v[26:27], v[26:27], v[26:27] op_sel:[0,1] op_sel_hi:[1,0]
	v_pk_add_f32 v[28:29], v[16:17], v[16:17] op_sel:[0,1] op_sel_hi:[1,0]
	v_pk_add_f32 v[30:31], v[18:19], v[18:19] op_sel:[0,1] op_sel_hi:[1,0]
	v_add_f32_e32 v24, 0, v1
	v_mov_b32_e32 v25, v20
	v_mov_b32_e32 v27, v21
	v_mov_b32_e32 v29, v22
	v_mov_b32_e32 v31, v23
	v_pk_add_f32 v[24:25], v[24:25], v[26:27]
	v_pk_add_f32 v[26:27], v[28:29], v[30:31]
	s_nop 0
	v_pk_add_f32 v[24:25], v[24:25], v[26:27]
	s_nop 0
	v_add_f32_e32 v1, v24, v25
	v_mbcnt_lo_u32_b32 v24, -1, 0
	v_mbcnt_hi_u32_b32 v24, -1, v24
	v_and_b32_e32 v25, 64, v24
	v_add_u32_e32 v25, 64, v25
	v_xor_b32_e32 v26, 32, v24
	v_cmp_lt_i32_e32 vcc, v26, v25
	s_nop 1
	v_cndmask_b32_e32 v26, v24, v26, vcc
	v_lshlrev_b32_e32 v52, 2, v26
	ds_bpermute_b32 v26, v52, v1
	s_waitcnt lgkmcnt(0)
	v_add_f32_e32 v1, v1, v26
	v_xor_b32_e32 v26, 16, v24
	v_cmp_lt_i32_e32 vcc, v26, v25
	s_nop 1
	v_cndmask_b32_e32 v26, v24, v26, vcc
	v_lshlrev_b32_e32 v53, 2, v26
	ds_bpermute_b32 v26, v53, v1
	s_waitcnt lgkmcnt(0)
	v_add_f32_e32 v1, v1, v26
	v_xor_b32_e32 v26, 8, v24
	v_cmp_lt_i32_e32 vcc, v26, v25
	s_nop 1
	v_cndmask_b32_e32 v26, v24, v26, vcc
	v_lshlrev_b32_e32 v54, 2, v26
	s_waitcnt lgkmcnt(0)
	s_nop 1
	v_add_f32_dpp v1, v1, v1 row_ror:8 row_mask:0xf bank_mask:0xf
	v_xor_b32_e32 v26, 4, v24
	v_cmp_lt_i32_e32 vcc, v26, v25
	s_nop 1
	v_cndmask_b32_e32 v26, v24, v26, vcc
	v_lshlrev_b32_e32 v55, 2, v26
	s_waitcnt lgkmcnt(0)
	s_nop 1
	v_add_f32_dpp v1, v1, v1 row_ror:4 row_mask:0xf bank_mask:0xf
	v_xor_b32_e32 v26, 2, v24
	v_cmp_lt_i32_e32 vcc, v26, v25
	s_nop 1
	v_cndmask_b32_e32 v26, v24, v26, vcc
	v_lshlrev_b32_e32 v56, 2, v26
	s_waitcnt lgkmcnt(0)
	s_nop 1
	v_add_f32_dpp v1, v1, v1 row_ror:2 row_mask:0xf bank_mask:0xf
	v_xor_b32_e32 v26, 1, v24
	v_cmp_lt_i32_e32 vcc, v26, v25
	s_nop 1
	v_cndmask_b32_e32 v24, v24, v26, vcc
	v_lshlrev_b32_e32 v57, 2, v24
	s_waitcnt lgkmcnt(0)
	s_nop 1
	v_add_f32_dpp v1, v1, v1 row_ror:1 row_mask:0xf bank_mask:0xf
	v_mul_f32_e32 v24, 0x3a800000, v1
	v_pk_add_f32 v[36:37], v[8:9], v[24:25] op_sel_hi:[1,0] neg_lo:[0,1] neg_hi:[0,1]
	v_pk_add_f32 v[38:39], v[10:11], v[24:25] op_sel_hi:[1,0] neg_lo:[0,1] neg_hi:[0,1]
	v_mov_b32_e32 v28, v37
	v_mov_b32_e32 v29, v39
	v_pk_add_f32 v[40:41], v[12:13], v[24:25] op_sel_hi:[1,0] neg_lo:[0,1] neg_hi:[0,1]
	v_pk_add_f32 v[42:43], v[14:15], v[24:25] op_sel_hi:[1,0] neg_lo:[0,1] neg_hi:[0,1]
	v_mov_b32_e32 v26, v36
	v_mov_b32_e32 v27, v38
	v_pk_mul_f32 v[28:29], v[28:29], v[28:29]
	v_mov_b32_e32 v30, v41
	v_mov_b32_e32 v31, v43
	v_pk_fma_f32 v[26:27], v[26:27], v[26:27], v[28:29]
	v_mov_b32_e32 v28, v40
	v_mov_b32_e32 v29, v42
	v_pk_mul_f32 v[30:31], v[30:31], v[30:31]
	v_pk_add_f32 v[44:45], v[16:17], v[24:25] op_sel_hi:[1,0] neg_lo:[0,1] neg_hi:[0,1]
	v_pk_fma_f32 v[28:29], v[28:29], v[28:29], v[30:31]
	v_mul_f32_e32 v30, v44, v44
	v_pk_fma_f32 v[30:31], v[44:45], v[44:45], v[30:31] op_sel_hi:[1,1,0]
	v_pk_add_f32 v[46:47], v[18:19], v[24:25] op_sel_hi:[1,0] neg_lo:[0,1] neg_hi:[0,1]
	v_pk_add_f32 v[48:49], v[20:21], v[24:25] op_sel_hi:[1,0] neg_lo:[0,1] neg_hi:[0,1]
	v_mul_f32_e32 v30, v46, v46
	v_pk_add_f32 v[50:51], v[22:23], v[24:25] op_sel_hi:[1,0] neg_lo:[0,1] neg_hi:[0,1]
	v_pk_fma_f32 v[32:33], v[46:47], v[46:47], v[30:31] op_sel_hi:[1,1,0]
	v_pk_mul_f32 v[34:35], v[48:49], v[48:49]
	v_pk_add_f32 v[26:27], v[26:27], v[26:27] op_sel_hi:[0,1]
	v_pk_add_f32 v[28:29], v[28:29], v[28:29] op_sel_hi:[0,1]
	v_pk_mul_f32 v[24:25], v[50:51], v[50:51]
	v_mov_b32_e32 v30, v34
	v_mov_b32_e32 v32, v35
	v_mov_b32_e32 v26, v24
	v_mov_b32_e32 v28, v25
	v_pk_add_f32 v[30:31], v[30:31], v[32:33]
	v_pk_add_f32 v[24:25], v[26:27], v[28:29]
	s_nop 0
	v_pk_add_f32 v[24:25], v[30:31], v[24:25]
	s_nop 0
	v_add_f32_e32 v1, v24, v25
	ds_bpermute_b32 v24, v52, v1
	s_waitcnt lgkmcnt(0)
	v_add_f32_e32 v1, v1, v24
	ds_bpermute_b32 v24, v53, v1
	s_waitcnt lgkmcnt(0)
	v_add_f32_e32 v1, v1, v24
	s_waitcnt lgkmcnt(0)
	s_nop 1
	v_add_f32_dpp v1, v1, v1 row_ror:8 row_mask:0xf bank_mask:0xf
	s_waitcnt lgkmcnt(0)
	s_nop 1
	v_add_f32_dpp v1, v1, v1 row_ror:4 row_mask:0xf bank_mask:0xf
	s_waitcnt vmcnt(0)
	v_mov_b32_e32 v24, v64
	v_mov_b32_e32 v25, v65
	v_mov_b32_e32 v26, v66
	v_mov_b32_e32 v27, v67
	v_mov_b32_e32 v28, v68
	v_mov_b32_e32 v29, v69
	v_mov_b32_e32 v30, v70
	v_mov_b32_e32 v31, v71
	s_waitcnt lgkmcnt(0)
	s_nop 1
	v_add_f32_dpp v1, v1, v1 row_ror:2 row_mask:0xf bank_mask:0xf
	global_store_dwordx4 v[6:7], v[8:11], off
	global_store_dwordx4 v[6:7], v[12:15], off offset:1024
	global_store_dwordx4 v[6:7], v[16:19], off offset:2048
	global_store_dwordx4 v[6:7], v[20:23], off offset:3072
	s_waitcnt lgkmcnt(0)
	s_nop 1
	v_add_f32_dpp v1, v1, v1 row_ror:1 row_mask:0xf bank_mask:0xf
	v_mov_b32_e32 v32, 0x3727c5ac
	v_fmac_f32_e32 v32, 0x3a800000, v1
	v_mul_f32_e32 v1, 0x4f800000, v32
	v_cmp_gt_f32_e32 vcc, s0, v32
	v_mov_b32_e32 v12, v80
	v_mov_b32_e32 v13, v81
	v_mov_b32_e32 v14, v82
	v_mov_b32_e32 v15, v83
	v_mov_b32_e32 v16, v84
	v_mov_b32_e32 v17, v85
	v_mov_b32_e32 v18, v86
	v_mov_b32_e32 v19, v87
	v_cndmask_b32_e32 v1, v32, v1, vcc
	v_sqrt_f32_e32 v32, v1
	v_mov_b32_e32 v8, v72
	v_mov_b32_e32 v9, v73
	v_mov_b32_e32 v10, v74
	v_mov_b32_e32 v11, v75
	v_add_u32_e32 v6, -1, v32
	v_fma_f32 v7, -v6, v32, v1
	v_cmp_ge_f32_e64 s[0:1], 0, v7
	v_add_u32_e32 v7, 1, v32
	v_fma_f32 v20, -v7, v32, v1
	v_cndmask_b32_e64 v6, v32, v6, s[0:1]
	v_cmp_lt_f32_e64 s[0:1], 0, v20
	v_mov_b32_e32 v20, v88
	v_mov_b32_e32 v21, v89
	v_mov_b32_e32 v22, v90
	v_mov_b32_e32 v23, v91
	s_nop 0
	v_cndmask_b32_e64 v6, v6, v7, s[0:1]
	v_mul_f32_e32 v7, 0x37800000, v6
	v_cndmask_b32_e32 v6, v6, v7, vcc
	v_mov_b32_e32 v7, 0x260
	v_cmp_class_f32_e32 vcc, v1, v7
	s_nop 1
	v_cndmask_b32_e32 v1, v6, v1, vcc
	v_div_scale_f32 v32, s[0:1], v1, v1, 1.0
	v_rcp_f32_e32 v33, v32
	v_lshl_add_u64 v[6:7], v[2:3], 0, v[4:5]
	v_div_scale_f32 v34, vcc, 1.0, v1, 1.0
	v_fma_f32 v2, -v32, v33, 1.0
	v_fmac_f32_e32 v33, v2, v33
	v_mul_f32_e32 v35, v34, v33
	v_fma_f32 v2, -v32, v35, v34
	v_fmac_f32_e32 v35, v2, v33
	v_fma_f32 v32, -v32, v35, v34
	v_mov_b32_e32 v2, v76
	v_mov_b32_e32 v3, v77
	v_mov_b32_e32 v4, v78
	v_mov_b32_e32 v5, v79
	v_div_fmas_f32 v52, v32, v33, v35
	v_mov_b32_e32 v32, v92
	v_mov_b32_e32 v33, v93
	v_mov_b32_e32 v34, v94
	v_mov_b32_e32 v35, v95
	v_div_fixup_f32 v0, v52, v1, 1.0
	v_pk_mul_f32 v[36:37], v[36:37], v[0:1] op_sel_hi:[1,0]
	s_waitcnt vmcnt(5)
	v_pk_fma_f32 v[12:13], v[24:25], v[36:37], v[12:13]
	v_pk_mul_f32 v[24:25], v[38:39], v[0:1] op_sel_hi:[1,0]
	v_cvt_pk_f16_f32 v12, v12, v13
	v_pk_fma_f32 v[14:15], v[26:27], v[24:25], v[14:15]
	s_nop 0
	v_cvt_pk_f16_f32 v13, v14, v15
	global_store_dwordx2 v[6:7], v[12:13], off
	v_pk_mul_f32 v[12:13], v[40:41], v[0:1] op_sel_hi:[1,0]
	v_pk_mul_f32 v[14:15], v[42:43], v[0:1] op_sel_hi:[1,0]
	s_waitcnt vmcnt(5)
	v_pk_fma_f32 v[12:13], v[28:29], v[12:13], v[16:17]
	v_pk_fma_f32 v[14:15], v[30:31], v[14:15], v[18:19]
	v_cvt_pk_f16_f32 v12, v12, v13
	v_cvt_pk_f16_f32 v13, v14, v15
	global_store_dwordx2 v[6:7], v[12:13], off offset:512
	v_pk_mul_f32 v[12:13], v[44:45], v[0:1] op_sel_hi:[1,0]
	s_waitcnt vmcnt(4)
	v_pk_fma_f32 v[8:9], v[12:13], v[8:9], v[20:21]
	v_pk_mul_f32 v[12:13], v[46:47], v[0:1] op_sel_hi:[1,0]
	v_cvt_pk_f16_f32 v8, v8, v9
	v_pk_fma_f32 v[10:11], v[12:13], v[10:11], v[22:23]
	s_nop 0
	v_cvt_pk_f16_f32 v9, v10, v11
	global_store_dwordx2 v[6:7], v[8:9], off offset:1024
	v_pk_mul_f32 v[8:9], v[48:49], v[0:1] op_sel_hi:[1,0]
	v_pk_mul_f32 v[0:1], v[50:51], v[0:1] op_sel_hi:[1,0]
	s_waitcnt vmcnt(3)
	v_pk_fma_f32 v[2:3], v[8:9], v[2:3], v[32:33]
	v_pk_fma_f32 v[0:1], v[0:1], v[4:5], v[34:35]
	v_cvt_pk_f16_f32 v2, v2, v3
	v_cvt_pk_f16_f32 v3, v0, v1
	global_store_dwordx2 v[6:7], v[2:3], off offset:1536
	s_endpgm
	s_endpgm
	s_endpgm
	s_endpgm
	s_endpgm
	s_endpgm
	s_endpgm
	s_endpgm
	s_endpgm
	s_endpgm
	s_endpgm
	s_endpgm
	s_endpgm
	s_endpgm
	s_endpgm
	s_endpgm
	s_endpgm
	s_endpgm
	s_endpgm
	s_endpgm
	s_endpgm
	s_endpgm
	s_endpgm
	s_endpgm
	s_endpgm
	s_endpgm
	s_endpgm
	s_endpgm
	s_endpgm
	s_endpgm
	s_endpgm
	s_endpgm
	s_endpgm
	s_endpgm
	s_endpgm
	s_endpgm
	s_endpgm
	s_endpgm
	s_endpgm
	s_endpgm
	s_endpgm

_Z9ln_kernelILi0EEvPKiPKfS3_PfS3_S3_PDF16_:
	s_load_dwordx4 s[12:15], s[0:1], 0x20
	v_and_b32_e32 v62, 63, v0
	v_lshlrev_b32_e32 v62, 4, v62
	s_load_dwordx8 s[4:11], s[0:1], 0x18
	v_and_b32_e32 v52, 63, v0
	v_lshrrev_b32_e32 v0, 6, v0
	v_lshl_or_b32 v0, s2, 2, v0
	v_ashrrev_i32_e32 v1, 31, v0
	v_lshlrev_b64 v[2:3], 12, v[0:1]
	s_waitcnt lgkmcnt(0)
	v_lshl_add_u64 v[4:5], s[4:5], 0, v[2:3]
	v_lshlrev_b32_e32 v2, 4, v52
	v_mov_b32_e32 v3, 0
	v_lshl_add_u64 v[20:21], v[4:5], 0, v[2:3]
	global_load_dwordx4 v[4:7], v[20:21], off offset:1024
	global_load_dwordx4 v[8:11], v[20:21], off offset:2048
	global_load_dwordx4 v[12:15], v[20:21], off
	global_load_dwordx4 v[16:19], v[20:21], off offset:3072
	global_load_dwordx4 v[64:67], v62, s[12:13]
	global_load_dwordx4 v[68:71], v62, s[12:13] offset:1024
	global_load_dwordx4 v[72:75], v62, s[12:13] offset:2048
	global_load_dwordx4 v[76:79], v62, s[12:13] offset:3072
	global_load_dwordx4 v[80:83], v62, s[14:15]
	global_load_dwordx4 v[84:87], v62, s[14:15] offset:1024
	global_load_dwordx4 v[88:91], v62, s[14:15] offset:2048
	global_load_dwordx4 v[92:95], v62, s[14:15] offset:3072
	v_mbcnt_lo_u32_b32 v20, -1, 0
	v_mbcnt_hi_u32_b32 v32, -1, v20
	v_and_b32_e32 v20, 64, v32
	v_xor_b32_e32 v21, 32, v32
	v_add_u32_e32 v34, 64, v20
	v_cmp_lt_i32_e32 vcc, v21, v34
	v_xor_b32_e32 v33, 16, v32
	s_mov_b32 s0, 0xf800000
	v_cndmask_b32_e32 v20, v32, v21, vcc
	v_lshlrev_b32_e32 v53, 2, v20
	v_cmp_lt_i32_e32 vcc, v33, v34
	v_lshlrev_b64 v[0:1], 11, v[0:1]
	v_lshl_add_u64 v[0:1], s[10:11], 0, v[0:1]
	s_waitcnt vmcnt(11)
	v_mov_b32_e32 v36, v5
	v_mov_b32_e32 v37, v6
	v_mov_b32_e32 v5, v7
	s_waitcnt vmcnt(9)
	v_mov_b32_e32 v22, v12
	v_mov_b32_e32 v23, v14
	v_mov_b32_e32 v24, v13
	v_mov_b32_e32 v25, v15
	v_mov_b32_e32 v6, v9
	v_mov_b32_e32 v20, v11
	s_waitcnt vmcnt(8)
	v_mov_b32_e32 v21, v16
	v_pk_add_f32 v[26:27], v[36:37], v[4:5]
	v_pk_add_f32 v[22:23], v[22:23], v[24:25]
	v_pk_add_f32 v[28:29], v[8:9], v[6:7]
	v_pk_add_f32 v[30:31], v[10:11], v[20:21]
	v_pk_add_f32 v[24:25], v[26:27], v[26:27] op_sel:[0,1] op_sel_hi:[1,0]
	v_add_f32_e32 v5, v22, v23
	v_mov_b32_e32 v29, v18
	v_mov_b32_e32 v31, v19
	v_add_f32_e32 v20, 0, v5
	v_mov_b32_e32 v25, v17
	v_pk_add_f32 v[22:23], v[28:29], v[30:31]
	v_pk_add_f32 v[20:21], v[20:21], v[24:25]
	v_pk_mov_b32 v[36:37], v[36:37], v[36:37] op_sel:[1,0]
	v_pk_add_f32 v[20:21], v[20:21], v[22:23]
	s_nop 0
	v_add_f32_e32 v5, v20, v21
	ds_bpermute_b32 v6, v53, v5
	v_cndmask_b32_e32 v21, v32, v33, vcc
	v_lshlrev_b32_e32 v54, 2, v21
	v_xor_b32_e32 v20, 8, v32
	v_cmp_lt_i32_e32 vcc, v20, v34
	s_waitcnt lgkmcnt(0)
	v_add_f32_e32 v5, v5, v6
	ds_bpermute_b32 v6, v54, v5
	v_cndmask_b32_e32 v20, v32, v20, vcc
	v_lshlrev_b32_e32 v55, 2, v20
	v_xor_b32_e32 v21, 4, v32
	v_cmp_lt_i32_e32 vcc, v21, v34
	s_waitcnt lgkmcnt(0)
	v_add_f32_e32 v5, v5, v6
	v_cndmask_b32_e32 v21, v32, v21, vcc
	v_lshlrev_b32_e32 v56, 2, v21
	v_xor_b32_e32 v20, 2, v32
	v_cmp_lt_i32_e32 vcc, v20, v34
	s_waitcnt lgkmcnt(0)
	s_nop 1
	v_add_f32_dpp v5, v5, v5 row_ror:8 row_mask:0xf bank_mask:0xf
	v_cndmask_b32_e32 v20, v32, v20, vcc
	v_lshlrev_b32_e32 v57, 2, v20
	v_xor_b32_e32 v21, 1, v32
	v_cmp_lt_i32_e32 vcc, v21, v34
	s_waitcnt lgkmcnt(0)
	s_nop 1
	v_add_f32_dpp v5, v5, v5 row_ror:4 row_mask:0xf bank_mask:0xf
	v_cndmask_b32_e32 v20, v32, v21, vcc
	v_lshlrev_b32_e32 v58, 2, v20
	s_waitcnt vmcnt(0)
	v_mov_b32_e32 v20, v64
	v_mov_b32_e32 v21, v65
	v_mov_b32_e32 v22, v66
	v_mov_b32_e32 v23, v67
	v_mov_b32_e32 v24, v80
	v_mov_b32_e32 v25, v81
	v_mov_b32_e32 v26, v82
	v_mov_b32_e32 v27, v83
	v_mov_b32_e32 v28, v68
	v_mov_b32_e32 v29, v69
	v_mov_b32_e32 v30, v70
	v_mov_b32_e32 v31, v71
	v_mov_b32_e32 v32, v84
	v_mov_b32_e32 v33, v85
	v_mov_b32_e32 v34, v86
	v_mov_b32_e32 v35, v87
	s_waitcnt lgkmcnt(0)
	s_nop 1
	v_add_f32_dpp v6, v5, v5 row_ror:2 row_mask:0xf bank_mask:0xf
	v_mov_b32_e32 v5, v37
	v_mov_b32_e32 v37, v7
	s_waitcnt lgkmcnt(0)
	s_nop 1
	v_add_f32_dpp v6, v6, v6 row_ror:1 row_mask:0xf bank_mask:0xf
	v_mul_f32_e32 v6, 0x3a800000, v6
	v_pk_add_f32 v[38:39], v[12:13], v[6:7] op_sel_hi:[1,0] neg_lo:[0,1] neg_hi:[0,1]
	v_pk_add_f32 v[40:41], v[14:15], v[6:7] op_sel_hi:[1,0] neg_lo:[0,1] neg_hi:[0,1]
	v_pk_add_f32 v[46:47], v[4:5], v[6:7] op_sel_hi:[1,0] neg_lo:[0,1] neg_hi:[0,1]
	v_pk_add_f32 v[36:37], v[36:37], v[6:7] op_sel_hi:[1,0] neg_lo:[0,1] neg_hi:[0,1]
	v_pk_add_f32 v[42:43], v[16:17], v[6:7] op_sel_hi:[1,0] neg_lo:[0,1] neg_hi:[0,1]
	v_pk_add_f32 v[44:45], v[18:19], v[6:7] op_sel_hi:[1,0] neg_lo:[0,1] neg_hi:[0,1]
	v_pk_add_f32 v[48:49], v[8:9], v[6:7] op_sel_hi:[1,0] neg_lo:[0,1] neg_hi:[0,1]
	v_pk_add_f32 v[50:51], v[10:11], v[6:7] op_sel_hi:[1,0] neg_lo:[0,1] neg_hi:[0,1]
	v_mov_b32_e32 v6, v39
	v_mov_b32_e32 v7, v41
	v_mov_b32_e32 v14, v47
	v_mov_b32_e32 v15, v37
	v_mov_b32_e32 v4, v38
	v_mov_b32_e32 v5, v40
	v_mov_b32_e32 v12, v46
	v_mov_b32_e32 v13, v36
	v_pk_mul_f32 v[6:7], v[6:7], v[6:7]
	v_pk_mul_f32 v[14:15], v[14:15], v[14:15]
	v_mul_f32_e32 v16, v48, v48
	v_mul_f32_e32 v18, v50, v50
	v_pk_fma_f32 v[4:5], v[4:5], v[4:5], v[6:7]
	v_pk_fma_f32 v[6:7], v[12:13], v[12:13], v[14:15]
	v_pk_mul_f32 v[8:9], v[42:43], v[42:43]
	v_pk_mul_f32 v[10:11], v[44:45], v[44:45]
	v_pk_fma_f32 v[16:17], v[48:49], v[48:49], v[16:17] op_sel_hi:[1,1,0]
	v_pk_fma_f32 v[18:19], v[50:51], v[50:51], v[18:19] op_sel_hi:[1,1,0]
	v_pk_add_f32 v[4:5], v[4:5], v[4:5] op_sel_hi:[0,1]
	v_pk_add_f32 v[6:7], v[6:7], v[6:7] op_sel_hi:[0,1]
	v_mov_b32_e32 v16, v8
	v_mov_b32_e32 v18, v9
	v_mov_b32_e32 v4, v10
	v_mov_b32_e32 v6, v11
	v_pk_add_f32 v[8:9], v[16:17], v[18:19]
	v_pk_add_f32 v[4:5], v[4:5], v[6:7]
	s_nop 0
	v_pk_add_f32 v[4:5], v[8:9], v[4:5]
	s_nop 0
	v_add_f32_e32 v59, v4, v5
	v_mov_b32_e32 v4, v72
	v_mov_b32_e32 v5, v73
	v_mov_b32_e32 v6, v74
	v_mov_b32_e32 v7, v75
	v_mov_b32_e32 v8, v88
	v_mov_b32_e32 v9, v89
	v_mov_b32_e32 v10, v90
	v_mov_b32_e32 v11, v91
	v_mov_b32_e32 v12, v76
	v_mov_b32_e32 v13, v77
	v_mov_b32_e32 v14, v78
	v_mov_b32_e32 v15, v79
	v_mov_b32_e32 v16, v92
	v_mov_b32_e32 v17, v93
	v_mov_b32_e32 v18, v94
	v_mov_b32_e32 v19, v95
	ds_bpermute_b32 v53, v53, v59
	s_waitcnt lgkmcnt(0)
	v_add_f32_e32 v2, v59, v53
	ds_bpermute_b32 v53, v54, v2
	v_mov_b32_e32 v54, 0x3727c5ac
	s_waitcnt lgkmcnt(0)
	v_add_f32_e32 v2, v2, v53
	v_mov_b32_e32 v55, 0x260
	s_waitcnt lgkmcnt(0)
	s_nop 1
	v_add_f32_dpp v2, v2, v2 row_ror:8 row_mask:0xf bank_mask:0xf
	s_waitcnt lgkmcnt(0)
	s_nop 1
	v_add_f32_dpp v2, v2, v2 row_ror:4 row_mask:0xf bank_mask:0xf
	s_waitcnt lgkmcnt(0)
	s_nop 1
	v_add_f32_dpp v2, v2, v2 row_ror:2 row_mask:0xf bank_mask:0xf
	s_waitcnt lgkmcnt(0)
	s_nop 1
	v_add_f32_dpp v2, v2, v2 row_ror:1 row_mask:0xf bank_mask:0xf
	v_fmac_f32_e32 v54, 0x3a800000, v2
	v_mul_f32_e32 v2, 0x4f800000, v54
	v_cmp_gt_f32_e32 vcc, s0, v54
	s_nop 1
	v_cndmask_b32_e32 v53, v54, v2, vcc
	v_sqrt_f32_e32 v54, v53
	v_lshlrev_b32_e32 v2, 3, v52
	v_lshl_add_u64 v[0:1], v[0:1], 0, v[2:3]
	v_add_u32_e32 v52, -1, v54
	v_add_u32_e32 v56, 1, v54
	v_fma_f32 v57, -v52, v54, v53
	v_fma_f32 v58, -v56, v54, v53
	v_cmp_ge_f32_e64 s[0:1], 0, v57
	s_nop 1
	v_cndmask_b32_e64 v52, v54, v52, s[0:1]
	v_cmp_lt_f32_e64 s[0:1], 0, v58
	s_nop 1
	v_cndmask_b32_e64 v52, v52, v56, s[0:1]
	v_mul_f32_e32 v54, 0x37800000, v52
	v_cndmask_b32_e32 v52, v52, v54, vcc
	v_cmp_class_f32_e32 vcc, v53, v55
	s_nop 1
	v_cndmask_b32_e32 v52, v52, v53, vcc
	v_div_scale_f32 v53, s[0:1], v52, v52, 1.0
	v_rcp_f32_e32 v54, v53
	v_div_scale_f32 v2, vcc, 1.0, v52, 1.0
	v_fma_f32 v3, -v53, v54, 1.0
	v_fmac_f32_e32 v54, v3, v54
	v_mul_f32_e32 v3, v2, v54
	v_fma_f32 v55, -v53, v3, v2
	v_fmac_f32_e32 v3, v55, v54
	v_fma_f32 v2, -v53, v3, v2
	v_div_fmas_f32 v2, v2, v54, v3
	v_div_fixup_f32 v2, v2, v52, 1.0
	v_pk_mul_f32 v[38:39], v[38:39], v[2:3] op_sel_hi:[1,0]
	v_pk_mul_f32 v[40:41], v[40:41], v[2:3] op_sel_hi:[1,0]
	v_pk_mul_f32 v[46:47], v[46:47], v[2:3] op_sel_hi:[1,0]
	v_pk_mul_f32 v[36:37], v[36:37], v[2:3] op_sel_hi:[1,0]
	v_pk_mul_f32 v[48:49], v[48:49], v[2:3] op_sel_hi:[1,0]
	v_pk_mul_f32 v[50:51], v[50:51], v[2:3] op_sel_hi:[1,0]
	v_pk_mul_f32 v[42:43], v[42:43], v[2:3] op_sel_hi:[1,0]
	v_pk_mul_f32 v[2:3], v[44:45], v[2:3] op_sel_hi:[1,0]
	s_waitcnt vmcnt(6)
	v_pk_fma_f32 v[20:21], v[20:21], v[38:39], v[24:25]
	v_pk_fma_f32 v[22:23], v[22:23], v[40:41], v[26:27]
	s_waitcnt vmcnt(4)
	v_pk_fma_f32 v[24:25], v[28:29], v[46:47], v[32:33]
	v_pk_fma_f32 v[26:27], v[30:31], v[36:37], v[34:35]
	s_waitcnt vmcnt(2)
	v_pk_fma_f32 v[4:5], v[48:49], v[4:5], v[8:9]
	v_pk_fma_f32 v[6:7], v[50:51], v[6:7], v[10:11]
	s_waitcnt vmcnt(0)
	v_pk_fma_f32 v[8:9], v[42:43], v[12:13], v[16:17]
	v_pk_fma_f32 v[2:3], v[2:3], v[14:15], v[18:19]
	v_cvt_pk_f16_f32 v10, v20, v21
	v_cvt_pk_f16_f32 v11, v22, v23
	v_cvt_pk_f16_f32 v12, v24, v25
	v_cvt_pk_f16_f32 v13, v26, v27
	v_cvt_pk_f16_f32 v4, v4, v5
	v_cvt_pk_f16_f32 v5, v6, v7
	v_cvt_pk_f16_f32 v6, v8, v9
	v_cvt_pk_f16_f32 v7, v2, v3
	global_store_dwordx2 v[0:1], v[10:11], off
	global_store_dwordx2 v[0:1], v[12:13], off offset:512
	global_store_dwordx2 v[0:1], v[4:5], off offset:1024
	global_store_dwordx2 v[0:1], v[6:7], off offset:1536
	s_endpgm
	s_endpgm
	s_endpgm
	s_endpgm
	s_endpgm
	s_endpgm
	s_endpgm
